# tail conversion v3: 3744 expert-weight items (layer 3 + 672 of layer 2) converted by idle CUs in the dense GEMM and MoE GEMM2 tail rounds
# speedup vs baseline: 1.0217x; 1.0035x over previous
.LBB0_55:
	s_cmp_lg_u32 s99, 0
	s_cbranch_scc1 .Ltc_itemdone
	v_readlane_b32 s2, v254, 0
	v_readlane_b32 s3, v254, 1
	s_load_dword s0, s[2:3], 0xe8
	s_add_i32 s14, s14, s15
	s_add_i32 s16, s16, s17
	s_add_i32 s10, s10, s18
	s_waitcnt lgkmcnt(0)
	s_add_i32 s22, s22, s0
	s_cmp_lt_i32 s22, 0x1560
	s_cbranch_scc1 .Ltc_noskip
	s_cmp_ge_i32 s22, 0x2000
	s_cbranch_scc1 .Ltc_noskip
	s_and_b32 s22, s22, 0xff
	s_addk_i32 s22, 0x2000
	s_lshl_b32 s14, s22, 5
	s_lshl_b32 s16, s22, 4
	s_lshl_b32 s10, s22, 9

.Ltc_next:
	s_cmp_ge_u32 s100, 0xea0
	s_cbranch_scc1 .Ltc_alldone
	s_movk_i32 s0, 0x2160
	s_cmp_lt_u32 s100, 0xaa0
	s_cselect_b32 s22, 0x1560, s0
	s_add_i32 s22, s22, s100
	v_mbcnt_lo_u32_b32 v0, -1, 0
	v_mbcnt_hi_u32_b32 v0, -1, v0
	s_and_b32 s0, s94, 0xffffffc0
	s_nop 0
	v_ashrrev_i32_e32 v1, 31, v0
	v_add_u32_e32 v2, s0, v0
	s_movk_i32 s0, 0x44
	v_lshlrev_b32_e32 v5, 7, v0
	v_mul_lo_u32 v4, v0, s0
	v_mul_lo_u32 v12, v2, s0
	v_lshrrev_b32_e32 v3, 1, v2
	v_and_b32_e32 v5, 0x80, v5
	s_movk_i32 s0, 0x7f
	v_and_or_b32 v3, v3, s0, v5
	s_lshl_b32 s6, s95, 3
	s_add_u32 s7, s88, 0x22000000
	s_addc_u32 s11, s89, 0
	v_add_u32_e32 v4, 0, v4
	s_add_u32 s12, s88, 0x2000000
	v_add_u32_e32 v4, s6, v4
	s_mov_b32 s1, 0
	s_addc_u32 s13, s89, 0
	s_lshl_b32 s14, s22, 5
	s_lshl_b32 s16, s22, 4
	s_lshl_b32 s10, s22, 9
	s_mov_b32 s19, 0xc3e00000
	s_movk_i32 s20, 0xff
	v_add_u32_e32 v5, 0x1100, v4
	v_add_u32_e32 v6, 0x2200, v4
	v_add_u32_e32 v7, 0x3300, v4
	v_add_u32_e32 v8, 0x4400, v4
	v_add_u32_e32 v9, 0x5500, v4
	v_add_u32_e32 v10, 0x6600, v4
	v_add_u32_e32 v11, 0x7700, v4
	v_add_u32_e32 v12, 0, v12
	s_movk_i32 s21, 0xff00
	v_mov_b32_e32 v13, 0x43e00000
	v_mov_b32_e32 v14, 8
	s_branch .LBB0_56

.Ltc_alldone:
	s_cmp_eq_u32 s99, 1
	s_cbranch_scc1 .Ltc_ret_1
	s_cmp_eq_u32 s99, 2
	s_cbranch_scc1 .Ltc_ret_2
	s_cmp_eq_u32 s99, 3
	s_cbranch_scc1 .Ltc_ret_3
	s_cmp_eq_u32 s99, 4
	s_cbranch_scc1 .Ltc_ret_4
	s_cmp_eq_u32 s99, 5
	s_cbranch_scc1 .Ltc_ret_5
	s_branch .Ltc_s1_fwd

.LBB0_668:
	s_cmp_lt_u32 s96, 144
	s_cbranch_scc1 .Ltc_skip_3
	v_writelane_b32 v200, s0, 0
	s_nop 1
	v_writelane_b32 v200, s1, 1
	s_nop 1
	v_writelane_b32 v200, s2, 2
	s_nop 1
	v_writelane_b32 v200, s3, 3
	s_nop 1
	v_writelane_b32 v200, s4, 4
	s_nop 1
	v_writelane_b32 v200, s5, 5
	s_nop 1
	v_writelane_b32 v200, s6, 6
	s_nop 1
	v_writelane_b32 v200, s7, 7
	s_nop 1
	v_writelane_b32 v200, s10, 8
	s_nop 1
	v_writelane_b32 v200, s11, 9
	s_nop 1
	v_writelane_b32 v200, s12, 10
	s_nop 1
	v_writelane_b32 v200, s13, 11
	s_nop 1
	v_writelane_b32 v200, s14, 12
	s_nop 1
	v_writelane_b32 v200, s15, 13
	s_nop 1
	v_writelane_b32 v200, s16, 14
	s_nop 1
	v_writelane_b32 v200, s17, 15
	s_nop 1
	v_writelane_b32 v200, s18, 16
	s_nop 1
	v_writelane_b32 v200, s19, 17
	s_nop 1
	v_writelane_b32 v200, s20, 18
	s_nop 1
	v_writelane_b32 v200, s21, 19
	s_nop 1
	v_writelane_b32 v200, s22, 20
	s_nop 1
	v_writelane_b32 v200, s23, 21
	s_nop 1
	v_writelane_b32 v200, s24, 22
	s_nop 1
	v_writelane_b32 v200, s25, 23
	s_nop 1
	v_writelane_b32 v200, s36, 24
	s_nop 1
	v_writelane_b32 v200, s37, 25
	s_nop 1
	v_writelane_b32 v200, s38, 26
	s_nop 1
	v_writelane_b32 v200, s39, 27
	s_nop 1
	v_writelane_b32 v200, s40, 28
	s_nop 1
	v_writelane_b32 v200, s41, 29
	s_nop 1
	v_writelane_b32 v200, s42, 30
	s_nop 1
	v_writelane_b32 v200, s43, 31
	s_nop 1
	v_writelane_b32 v200, s44, 32
	s_nop 1
	v_writelane_b32 v200, s45, 33
	s_nop 1
	v_writelane_b32 v200, s46, 34
	s_nop 1
	v_writelane_b32 v200, s47, 35
	s_nop 1
	v_writelane_b32 v200, s48, 36
	s_nop 1
	v_writelane_b32 v200, s49, 37
	s_nop 1
	v_writelane_b32 v200, s50, 38
	s_nop 1
	v_writelane_b32 v200, s51, 39
	s_nop 1
	s_mov_b32 s99, 3
	s_mov_b32 s98, 2
	s_mov_b32 s101, 112
	s_add_i32 s100, s96, 752
	s_branch .Ltc_next
.Ltc_ret_3:
	s_mov_b32 s99, 0
	v_readlane_b32 s0, v200, 0
	v_readlane_b32 s1, v200, 1
	v_readlane_b32 s2, v200, 2
	v_readlane_b32 s3, v200, 3
	v_readlane_b32 s4, v200, 4
	v_readlane_b32 s5, v200, 5
	v_readlane_b32 s6, v200, 6
	v_readlane_b32 s7, v200, 7
	v_readlane_b32 s10, v200, 8
	v_readlane_b32 s11, v200, 9
	v_readlane_b32 s12, v200, 10
	v_readlane_b32 s13, v200, 11
	v_readlane_b32 s14, v200, 12
	v_readlane_b32 s15, v200, 13
	v_readlane_b32 s16, v200, 14
	v_readlane_b32 s17, v200, 15
	v_readlane_b32 s18, v200, 16
	v_readlane_b32 s19, v200, 17
	v_readlane_b32 s20, v200, 18
	v_readlane_b32 s21, v200, 19
	v_readlane_b32 s22, v200, 20
	v_readlane_b32 s23, v200, 21
	v_readlane_b32 s24, v200, 22
	v_readlane_b32 s25, v200, 23
	v_readlane_b32 s36, v200, 24
	v_readlane_b32 s37, v200, 25
	v_readlane_b32 s38, v200, 26
	v_readlane_b32 s39, v200, 27
	v_readlane_b32 s40, v200, 28
	v_readlane_b32 s41, v200, 29
	v_readlane_b32 s42, v200, 30
	v_readlane_b32 s43, v200, 31
	v_readlane_b32 s44, v200, 32
	v_readlane_b32 s45, v200, 33
	v_readlane_b32 s46, v200, 34
	v_readlane_b32 s47, v200, 35
	v_readlane_b32 s48, v200, 36
	v_readlane_b32 s49, v200, 37
	v_readlane_b32 s50, v200, 38
	v_readlane_b32 s51, v200, 39
	s_nop 1
.Ltc_skip_3:
	v_readlane_b32 s0, v254, 0
	v_readlane_b32 s1, v254, 1
	s_load_dwordx2 s[0:1], s[0:1], 0xd8
	s_waitcnt lgkmcnt(0)
	s_cmp_gt_i32 s1, 8
	s_cselect_b64 s[0:1], -1, 0
	s_and_b64 s[2:3], s[4:5], s[0:1]
	s_andn2_b64 vcc, exec, s[2:3]
	s_cbranch_vccnz .LBB0_724
	s_waitcnt vmcnt(0)
	s_cmp_gt_u32 s94, 63
	s_barrier
	s_cbranch_scc1 .LBB0_723
	v_mbcnt_lo_u32_b32 v0, -1, 0
	v_mbcnt_hi_u32_b32 v0, -1, v0
	v_cmp_eq_u32_e32 vcc, 0, v0
	s_and_saveexec_b64 s[2:3], vcc
	s_cbranch_execz .LBB0_722
	s_add_i32 s4, 0, 0x20020
	v_mov_b32_e32 v0, s4
	s_waitcnt vmcnt(0) expcnt(0) lgkmcnt(0)
	ds_read_b32 v2, v0
	s_add_i32 s4, 0, 0x20024
	v_mov_b32_e32 v0, s4
	ds_read_b32 v0, v0
	s_waitcnt lgkmcnt(1)
	v_cmp_ne_u32_e32 vcc, 0, v2
	s_cbranch_vccnz .LBB0_686
	v_readlane_b32 s4, v254, 2
	v_readlane_b32 s10, v254, 0
	v_readlane_b32 s5, v254, 3
	v_readlane_b32 s11, v254, 1
	s_load_dwordx2 s[8:9], s[4:5], 0x4
	s_mov_b32 s46, 1
	s_load_dword s10, s[10:11], 0xe8
	s_add_u32 s4, s88, 0x4200
	s_addc_u32 s5, s89, 0
	s_add_u32 s6, s88, 0x4400
	s_addc_u32 s7, s89, 0
	s_waitcnt lgkmcnt(0)
	s_mul_i32 s33, s8, s10
	s_add_u32 s8, s88, 0x4500
	s_mul_i32 s33, s33, s9
	s_addc_u32 s9, s89, 0
	s_add_u32 s10, s88, 0x4600
	s_addc_u32 s11, s89, 0
	s_add_u32 s12, s88, 0x4700
	s_addc_u32 s13, s89, 0
	s_add_u32 s14, s88, 0x4800
	s_addc_u32 s15, s89, 0
	s_add_u32 s16, s88, 0x4900
	s_addc_u32 s17, s89, 0
	s_add_u32 s18, s88, 0x4a00
	s_addc_u32 s19, s89, 0
	s_add_u32 s20, s88, 0x4b00
	s_addc_u32 s21, s89, 0
	s_add_u32 s22, s88, 0x4c00
	s_addc_u32 s23, s89, 0
	s_add_u32 s24, s88, 0x4d00
	s_addc_u32 s25, s89, 0
	s_add_u32 s26, s88, 0x4e00
	s_addc_u32 s27, s89, 0
	s_add_u32 s28, s88, 0x4f00
	s_addc_u32 s29, s89, 0
	s_add_u32 s30, s88, 0x5000
	s_addc_u32 s31, s89, 0
	s_add_u32 s34, s88, 0x5100
	s_addc_u32 s35, s89, 0
	s_add_u32 s36, s88, 0x5200
	s_addc_u32 s37, s89, 0
	s_add_u32 s38, s88, 0x5300
	s_addc_u32 s39, s89, 0
	v_mov_b32_e32 v16, 0
	s_branch .LBB0_674

.LBB0_807:
	s_cmp_lt_u32 s96, 48
	s_cbranch_scc1 .Ltc_skip_4
	v_writelane_b32 v200, s0, 0
	s_nop 1
	v_writelane_b32 v200, s1, 1
	s_nop 1
	v_writelane_b32 v200, s2, 2
	s_nop 1
	v_writelane_b32 v200, s3, 3
	s_nop 1
	v_writelane_b32 v200, s4, 4
	s_nop 1
	v_writelane_b32 v200, s5, 5
	s_nop 1
	v_writelane_b32 v200, s6, 6
	s_nop 1
	v_writelane_b32 v200, s7, 7
	s_nop 1
	v_writelane_b32 v200, s10, 8
	s_nop 1
	v_writelane_b32 v200, s11, 9
	s_nop 1
	v_writelane_b32 v200, s12, 10
	s_nop 1
	v_writelane_b32 v200, s13, 11
	s_nop 1
	v_writelane_b32 v200, s14, 12
	s_nop 1
	v_writelane_b32 v200, s15, 13
	s_nop 1
	v_writelane_b32 v200, s16, 14
	s_nop 1
	v_writelane_b32 v200, s17, 15
	s_nop 1
	v_writelane_b32 v200, s18, 16
	s_nop 1
	v_writelane_b32 v200, s19, 17
	s_nop 1
	v_writelane_b32 v200, s20, 18
	s_nop 1
	v_writelane_b32 v200, s21, 19
	s_nop 1
	v_writelane_b32 v200, s22, 20
	s_nop 1
	v_writelane_b32 v200, s23, 21
	s_nop 1
	v_writelane_b32 v200, s24, 22
	s_nop 1
	v_writelane_b32 v200, s25, 23
	s_nop 1
	v_writelane_b32 v200, s36, 24
	s_nop 1
	v_writelane_b32 v200, s37, 25
	s_nop 1
	v_writelane_b32 v200, s38, 26
	s_nop 1
	v_writelane_b32 v200, s39, 27
	s_nop 1
	v_writelane_b32 v200, s40, 28
	s_nop 1
	v_writelane_b32 v200, s41, 29
	s_nop 1
	v_writelane_b32 v200, s42, 30
	s_nop 1
	v_writelane_b32 v200, s43, 31
	s_nop 1
	v_writelane_b32 v200, s44, 32
	s_nop 1
	v_writelane_b32 v200, s45, 33
	s_nop 1
	v_writelane_b32 v200, s46, 34
	s_nop 1
	v_writelane_b32 v200, s47, 35
	s_nop 1
	v_writelane_b32 v200, s48, 36
	s_nop 1
	v_writelane_b32 v200, s49, 37
	s_nop 1
	v_writelane_b32 v200, s50, 38
	s_nop 1
	v_writelane_b32 v200, s51, 39
	s_nop 1
	s_mov_b32 s99, 4
	s_mov_b32 s98, 2
	s_mov_b32 s101, 208
	s_add_i32 s100, s96, 1072
	s_branch .Ltc_next

.Ltc_s1_fwd:
	s_cmp_eq_u32 s99, 6
	s_cbranch_scc1 .Ltc_ret_6
	s_cmp_eq_u32 s99, 7
	s_cbranch_scc1 .Ltc_ret_7
	s_cmp_eq_u32 s99, 8
	s_cbranch_scc1 .Ltc_ret_8
	s_branch .Ltc_s2_fwd

.LBB0_1052:
	s_cmp_lt_u32 s96, 32
	s_cbranch_scc1 .Ltc_skip_5
	v_writelane_b32 v200, s0, 0
	s_nop 1
	v_writelane_b32 v200, s1, 1
	s_nop 1
	v_writelane_b32 v200, s2, 2
	s_nop 1
	v_writelane_b32 v200, s3, 3
	s_nop 1
	v_writelane_b32 v200, s4, 4
	s_nop 1
	v_writelane_b32 v200, s5, 5
	s_nop 1
	v_writelane_b32 v200, s6, 6
	s_nop 1
	v_writelane_b32 v200, s7, 7
	s_nop 1
	v_writelane_b32 v200, s10, 8
	s_nop 1
	v_writelane_b32 v200, s11, 9
	s_nop 1
	v_writelane_b32 v200, s12, 10
	s_nop 1
	v_writelane_b32 v200, s13, 11
	s_nop 1
	v_writelane_b32 v200, s14, 12
	s_nop 1
	v_writelane_b32 v200, s15, 13
	s_nop 1
	v_writelane_b32 v200, s16, 14
	s_nop 1
	v_writelane_b32 v200, s17, 15
	s_nop 1
	v_writelane_b32 v200, s18, 16
	s_nop 1
	v_writelane_b32 v200, s19, 17
	s_nop 1
	v_writelane_b32 v200, s20, 18
	s_nop 1
	v_writelane_b32 v200, s21, 19
	s_nop 1
	v_writelane_b32 v200, s22, 20
	s_nop 1
	v_writelane_b32 v200, s23, 21
	s_nop 1
	v_writelane_b32 v200, s24, 22
	s_nop 1
	v_writelane_b32 v200, s25, 23
	s_nop 1
	v_writelane_b32 v200, s36, 24
	s_nop 1
	v_writelane_b32 v200, s37, 25
	s_nop 1
	v_writelane_b32 v200, s38, 26
	s_nop 1
	v_writelane_b32 v200, s39, 27
	s_nop 1
	v_writelane_b32 v200, s40, 28
	s_nop 1
	v_writelane_b32 v200, s41, 29
	s_nop 1
	v_writelane_b32 v200, s42, 30
	s_nop 1
	v_writelane_b32 v200, s43, 31
	s_nop 1
	v_writelane_b32 v200, s44, 32
	s_nop 1
	v_writelane_b32 v200, s45, 33
	s_nop 1
	v_writelane_b32 v200, s46, 34
	s_nop 1
	v_writelane_b32 v200, s47, 35
	s_nop 1
	v_writelane_b32 v200, s48, 36
	s_nop 1
	v_writelane_b32 v200, s49, 37
	s_nop 1
	v_writelane_b32 v200, s50, 38
	s_nop 1
	v_writelane_b32 v200, s51, 39
	s_nop 1
	s_mov_b32 s99, 5
	s_mov_b32 s98, 2
	s_mov_b32 s101, 224
	s_add_i32 s100, s96, 1504
	s_branch .Ltc_next

.LBB0_1361:
	s_cmp_lt_u32 s96, 144
	s_cbranch_scc1 .Ltc_skip_6
	v_writelane_b32 v200, s0, 0
	s_nop 1
	v_writelane_b32 v200, s1, 1
	s_nop 1
	v_writelane_b32 v200, s2, 2
	s_nop 1
	v_writelane_b32 v200, s3, 3
	s_nop 1
	v_writelane_b32 v200, s4, 4
	s_nop 1
	v_writelane_b32 v200, s5, 5
	s_nop 1
	v_writelane_b32 v200, s6, 6
	s_nop 1
	v_writelane_b32 v200, s7, 7
	s_nop 1
	v_writelane_b32 v200, s10, 8
	s_nop 1
	v_writelane_b32 v200, s11, 9
	s_nop 1
	v_writelane_b32 v200, s12, 10
	s_nop 1
	v_writelane_b32 v200, s13, 11
	s_nop 1
	v_writelane_b32 v200, s14, 12
	s_nop 1
	v_writelane_b32 v200, s15, 13
	s_nop 1
	v_writelane_b32 v200, s16, 14
	s_nop 1
	v_writelane_b32 v200, s17, 15
	s_nop 1
	v_writelane_b32 v200, s18, 16
	s_nop 1
	v_writelane_b32 v200, s19, 17
	s_nop 1
	v_writelane_b32 v200, s20, 18
	s_nop 1
	v_writelane_b32 v200, s21, 19
	s_nop 1
	v_writelane_b32 v200, s22, 20
	s_nop 1
	v_writelane_b32 v200, s23, 21
	s_nop 1
	v_writelane_b32 v200, s24, 22
	s_nop 1
	v_writelane_b32 v200, s25, 23
	s_nop 1
	v_writelane_b32 v200, s36, 24
	s_nop 1
	v_writelane_b32 v200, s37, 25
	s_nop 1
	v_writelane_b32 v200, s38, 26
	s_nop 1
	v_writelane_b32 v200, s39, 27
	s_nop 1
	v_writelane_b32 v200, s40, 28
	s_nop 1
	v_writelane_b32 v200, s41, 29
	s_nop 1
	v_writelane_b32 v200, s42, 30
	s_nop 1
	v_writelane_b32 v200, s43, 31
	s_nop 1
	v_writelane_b32 v200, s44, 32
	s_nop 1
	v_writelane_b32 v200, s45, 33
	s_nop 1
	v_writelane_b32 v200, s46, 34
	s_nop 1
	v_writelane_b32 v200, s47, 35
	s_nop 1
	v_writelane_b32 v200, s48, 36
	s_nop 1
	v_writelane_b32 v200, s49, 37
	s_nop 1
	v_writelane_b32 v200, s50, 38
	s_nop 1
	v_writelane_b32 v200, s51, 39
	s_nop 1
	s_mov_b32 s99, 6
	s_mov_b32 s98, 2
	s_mov_b32 s101, 112
	s_add_i32 s100, s96, 1840
	s_branch .Ltc_s1_back
.Ltc_ret_6:
	s_mov_b32 s99, 0
	v_readlane_b32 s0, v200, 0
	v_readlane_b32 s1, v200, 1
	v_readlane_b32 s2, v200, 2
	v_readlane_b32 s3, v200, 3
	v_readlane_b32 s4, v200, 4
	v_readlane_b32 s5, v200, 5
	v_readlane_b32 s6, v200, 6
	v_readlane_b32 s7, v200, 7
	v_readlane_b32 s10, v200, 8
	v_readlane_b32 s11, v200, 9
	v_readlane_b32 s12, v200, 10
	v_readlane_b32 s13, v200, 11
	v_readlane_b32 s14, v200, 12
	v_readlane_b32 s15, v200, 13
	v_readlane_b32 s16, v200, 14
	v_readlane_b32 s17, v200, 15
	v_readlane_b32 s18, v200, 16
	v_readlane_b32 s19, v200, 17
	v_readlane_b32 s20, v200, 18
	v_readlane_b32 s21, v200, 19
	v_readlane_b32 s22, v200, 20
	v_readlane_b32 s23, v200, 21
	v_readlane_b32 s24, v200, 22
	v_readlane_b32 s25, v200, 23
	v_readlane_b32 s36, v200, 24
	v_readlane_b32 s37, v200, 25
	v_readlane_b32 s38, v200, 26
	v_readlane_b32 s39, v200, 27
	v_readlane_b32 s40, v200, 28
	v_readlane_b32 s41, v200, 29
	v_readlane_b32 s42, v200, 30
	v_readlane_b32 s43, v200, 31
	v_readlane_b32 s44, v200, 32
	v_readlane_b32 s45, v200, 33
	v_readlane_b32 s46, v200, 34
	v_readlane_b32 s47, v200, 35
	v_readlane_b32 s48, v200, 36
	v_readlane_b32 s49, v200, 37
	v_readlane_b32 s50, v200, 38
	v_readlane_b32 s51, v200, 39
	s_nop 1
.Ltc_skip_6:
	v_readlane_b32 s0, v254, 0
	v_readlane_b32 s1, v254, 1
	s_load_dwordx2 s[0:1], s[0:1], 0xd8
	s_waitcnt lgkmcnt(0)
	s_cmp_gt_i32 s1, 16
	s_cselect_b64 s[0:1], -1, 0
	s_and_b64 s[2:3], s[4:5], s[0:1]
	s_andn2_b64 vcc, exec, s[2:3]
	s_cbranch_vccnz .LBB0_1417
	s_waitcnt vmcnt(0)
	s_cmp_gt_u32 s94, 63
	s_barrier
	s_cbranch_scc1 .LBB0_1416
	v_mbcnt_lo_u32_b32 v0, -1, 0
	v_mbcnt_hi_u32_b32 v0, -1, v0
	v_cmp_eq_u32_e32 vcc, 0, v0
	s_and_saveexec_b64 s[2:3], vcc
	s_cbranch_execz .LBB0_1415
	s_add_i32 s4, 0, 0x20020
	v_mov_b32_e32 v0, s4
	s_waitcnt vmcnt(0) expcnt(0) lgkmcnt(0)
	ds_read_b32 v2, v0
	s_add_i32 s4, 0, 0x20024
	v_mov_b32_e32 v0, s4
	ds_read_b32 v0, v0
	s_waitcnt lgkmcnt(1)
	v_cmp_ne_u32_e32 vcc, 0, v2
	s_cbranch_vccnz .LBB0_1379
	v_readlane_b32 s4, v254, 2
	v_readlane_b32 s10, v254, 0
	v_readlane_b32 s5, v254, 3
	v_readlane_b32 s11, v254, 1
	s_load_dwordx2 s[8:9], s[4:5], 0x4
	s_mov_b32 s46, 1
	s_load_dword s10, s[10:11], 0xe8
	s_add_u32 s4, s88, 0x4200
	s_addc_u32 s5, s89, 0
	s_add_u32 s6, s88, 0x4400
	s_addc_u32 s7, s89, 0
	s_waitcnt lgkmcnt(0)
	s_mul_i32 s33, s8, s10
	s_add_u32 s8, s88, 0x4500
	s_mul_i32 s33, s33, s9
	s_addc_u32 s9, s89, 0
	s_add_u32 s10, s88, 0x4600
	s_addc_u32 s11, s89, 0
	s_add_u32 s12, s88, 0x4700
	s_addc_u32 s13, s89, 0
	s_add_u32 s14, s88, 0x4800
	s_addc_u32 s15, s89, 0
	s_add_u32 s16, s88, 0x4900
	s_addc_u32 s17, s89, 0
	s_add_u32 s18, s88, 0x4a00
	s_addc_u32 s19, s89, 0
	s_add_u32 s20, s88, 0x4b00
	s_addc_u32 s21, s89, 0
	s_add_u32 s22, s88, 0x4c00
	s_addc_u32 s23, s89, 0
	s_add_u32 s24, s88, 0x4d00
	s_addc_u32 s25, s89, 0
	s_add_u32 s26, s88, 0x4e00
	s_addc_u32 s27, s89, 0
	s_add_u32 s28, s88, 0x4f00
	s_addc_u32 s29, s89, 0
	s_add_u32 s30, s88, 0x5000
	s_addc_u32 s31, s89, 0
	s_add_u32 s34, s88, 0x5100
	s_addc_u32 s35, s89, 0
	s_add_u32 s36, s88, 0x5200
	s_addc_u32 s37, s89, 0
	s_add_u32 s38, s88, 0x5300
	s_addc_u32 s39, s89, 0
	v_mov_b32_e32 v16, 0
	s_branch .LBB0_1367

.LBB0_1495:
	s_cmp_lt_u32 s96, 48
	s_cbranch_scc1 .Ltc_skip_7
	v_writelane_b32 v200, s0, 0
	s_nop 1
	v_writelane_b32 v200, s1, 1
	s_nop 1
	v_writelane_b32 v200, s2, 2
	s_nop 1
	v_writelane_b32 v200, s3, 3
	s_nop 1
	v_writelane_b32 v200, s4, 4
	s_nop 1
	v_writelane_b32 v200, s5, 5
	s_nop 1
	v_writelane_b32 v200, s6, 6
	s_nop 1
	v_writelane_b32 v200, s7, 7
	s_nop 1
	v_writelane_b32 v200, s10, 8
	s_nop 1
	v_writelane_b32 v200, s11, 9
	s_nop 1
	v_writelane_b32 v200, s12, 10
	s_nop 1
	v_writelane_b32 v200, s13, 11
	s_nop 1
	v_writelane_b32 v200, s14, 12
	s_nop 1
	v_writelane_b32 v200, s15, 13
	s_nop 1
	v_writelane_b32 v200, s16, 14
	s_nop 1
	v_writelane_b32 v200, s17, 15
	s_nop 1
	v_writelane_b32 v200, s18, 16
	s_nop 1
	v_writelane_b32 v200, s19, 17
	s_nop 1
	v_writelane_b32 v200, s20, 18
	s_nop 1
	v_writelane_b32 v200, s21, 19
	s_nop 1
	v_writelane_b32 v200, s22, 20
	s_nop 1
	v_writelane_b32 v200, s23, 21
	s_nop 1
	v_writelane_b32 v200, s24, 22
	s_nop 1
	v_writelane_b32 v200, s25, 23
	s_nop 1
	v_writelane_b32 v200, s36, 24
	s_nop 1
	v_writelane_b32 v200, s37, 25
	s_nop 1
	v_writelane_b32 v200, s38, 26
	s_nop 1
	v_writelane_b32 v200, s39, 27
	s_nop 1
	v_writelane_b32 v200, s40, 28
	s_nop 1
	v_writelane_b32 v200, s41, 29
	s_nop 1
	v_writelane_b32 v200, s42, 30
	s_nop 1
	v_writelane_b32 v200, s43, 31
	s_nop 1
	v_writelane_b32 v200, s44, 32
	s_nop 1
	v_writelane_b32 v200, s45, 33
	s_nop 1
	v_writelane_b32 v200, s46, 34
	s_nop 1
	v_writelane_b32 v200, s47, 35
	s_nop 1
	v_writelane_b32 v200, s48, 36
	s_nop 1
	v_writelane_b32 v200, s49, 37
	s_nop 1
	v_writelane_b32 v200, s50, 38
	s_nop 1
	v_writelane_b32 v200, s51, 39
	s_nop 1
	s_mov_b32 s99, 7
	s_mov_b32 s98, 2
	s_mov_b32 s101, 208
	s_add_i32 s100, s96, 2160
	s_branch .Ltc_s1_back

.LBB0_1711:
	s_cmp_lt_u32 s96, 32
	s_cbranch_scc1 .Ltc_skip_8
	v_writelane_b32 v200, s0, 0
	s_nop 1
	v_writelane_b32 v200, s1, 1
	s_nop 1
	v_writelane_b32 v200, s2, 2
	s_nop 1
	v_writelane_b32 v200, s3, 3
	s_nop 1
	v_writelane_b32 v200, s4, 4
	s_nop 1
	v_writelane_b32 v200, s5, 5
	s_nop 1
	v_writelane_b32 v200, s6, 6
	s_nop 1
	v_writelane_b32 v200, s7, 7
	s_nop 1
	v_writelane_b32 v200, s10, 8
	s_nop 1
	v_writelane_b32 v200, s11, 9
	s_nop 1
	v_writelane_b32 v200, s12, 10
	s_nop 1
	v_writelane_b32 v200, s13, 11
	s_nop 1
	v_writelane_b32 v200, s14, 12
	s_nop 1
	v_writelane_b32 v200, s15, 13
	s_nop 1
	v_writelane_b32 v200, s16, 14
	s_nop 1
	v_writelane_b32 v200, s17, 15
	s_nop 1
	v_writelane_b32 v200, s18, 16
	s_nop 1
	v_writelane_b32 v200, s19, 17
	s_nop 1
	v_writelane_b32 v200, s20, 18
	s_nop 1
	v_writelane_b32 v200, s21, 19
	s_nop 1
	v_writelane_b32 v200, s22, 20
	s_nop 1
	v_writelane_b32 v200, s23, 21
	s_nop 1
	v_writelane_b32 v200, s24, 22
	s_nop 1
	v_writelane_b32 v200, s25, 23
	s_nop 1
	v_writelane_b32 v200, s36, 24
	s_nop 1
	v_writelane_b32 v200, s37, 25
	s_nop 1
	v_writelane_b32 v200, s38, 26
	s_nop 1
	v_writelane_b32 v200, s39, 27
	s_nop 1
	v_writelane_b32 v200, s40, 28
	s_nop 1
	v_writelane_b32 v200, s41, 29
	s_nop 1
	v_writelane_b32 v200, s42, 30
	s_nop 1
	v_writelane_b32 v200, s43, 31
	s_nop 1
	v_writelane_b32 v200, s44, 32
	s_nop 1
	v_writelane_b32 v200, s45, 33
	s_nop 1
	v_writelane_b32 v200, s46, 34
	s_nop 1
	v_writelane_b32 v200, s47, 35
	s_nop 1
	v_writelane_b32 v200, s48, 36
	s_nop 1
	v_writelane_b32 v200, s49, 37
	s_nop 1
	v_writelane_b32 v200, s50, 38
	s_nop 1
	v_writelane_b32 v200, s51, 39
	s_nop 1
	s_mov_b32 s99, 8
	s_mov_b32 s98, 2
	s_mov_b32 s101, 224
	s_add_i32 s100, s96, 2592
	s_branch .Ltc_s1_back

.Ltc_s2_fwd:
	s_cmp_eq_u32 s99, 9
	s_cbranch_scc1 .Ltc_ret_9
	s_branch .Ltc_ret_10

.LBB0_2020:
	s_cmp_lt_u32 s96, 144
	s_cbranch_scc1 .Ltc_skip_9
	v_writelane_b32 v200, s0, 0
	s_nop 1
	v_writelane_b32 v200, s1, 1
	s_nop 1
	v_writelane_b32 v200, s2, 2
	s_nop 1
	v_writelane_b32 v200, s3, 3
	s_nop 1
	v_writelane_b32 v200, s4, 4
	s_nop 1
	v_writelane_b32 v200, s5, 5
	s_nop 1
	v_writelane_b32 v200, s6, 6
	s_nop 1
	v_writelane_b32 v200, s7, 7
	s_nop 1
	v_writelane_b32 v200, s10, 8
	s_nop 1
	v_writelane_b32 v200, s11, 9
	s_nop 1
	v_writelane_b32 v200, s12, 10
	s_nop 1
	v_writelane_b32 v200, s13, 11
	s_nop 1
	v_writelane_b32 v200, s14, 12
	s_nop 1
	v_writelane_b32 v200, s15, 13
	s_nop 1
	v_writelane_b32 v200, s16, 14
	s_nop 1
	v_writelane_b32 v200, s17, 15
	s_nop 1
	v_writelane_b32 v200, s18, 16
	s_nop 1
	v_writelane_b32 v200, s19, 17
	s_nop 1
	v_writelane_b32 v200, s20, 18
	s_nop 1
	v_writelane_b32 v200, s21, 19
	s_nop 1
	v_writelane_b32 v200, s22, 20
	s_nop 1
	v_writelane_b32 v200, s23, 21
	s_nop 1
	v_writelane_b32 v200, s24, 22
	s_nop 1
	v_writelane_b32 v200, s25, 23
	s_nop 1
	v_writelane_b32 v200, s36, 24
	s_nop 1
	v_writelane_b32 v200, s37, 25
	s_nop 1
	v_writelane_b32 v200, s38, 26
	s_nop 1
	v_writelane_b32 v200, s39, 27
	s_nop 1
	v_writelane_b32 v200, s40, 28
	s_nop 1
	v_writelane_b32 v200, s41, 29
	s_nop 1
	v_writelane_b32 v200, s42, 30
	s_nop 1
	v_writelane_b32 v200, s43, 31
	s_nop 1
	v_writelane_b32 v200, s44, 32
	s_nop 1
	v_writelane_b32 v200, s45, 33
	s_nop 1
	v_writelane_b32 v200, s46, 34
	s_nop 1
	v_writelane_b32 v200, s47, 35
	s_nop 1
	v_writelane_b32 v200, s48, 36
	s_nop 1
	v_writelane_b32 v200, s49, 37
	s_nop 1
	v_writelane_b32 v200, s50, 38
	s_nop 1
	v_writelane_b32 v200, s51, 39
	s_nop 1
	s_mov_b32 s99, 9
	s_mov_b32 s98, 2
	s_mov_b32 s101, 112
	s_add_i32 s100, s96, 2928
	s_branch .Ltc_s2_back
.Ltc_ret_9:
	s_mov_b32 s99, 0
	v_readlane_b32 s0, v200, 0
	v_readlane_b32 s1, v200, 1
	v_readlane_b32 s2, v200, 2
	v_readlane_b32 s3, v200, 3
	v_readlane_b32 s4, v200, 4
	v_readlane_b32 s5, v200, 5
	v_readlane_b32 s6, v200, 6
	v_readlane_b32 s7, v200, 7
	v_readlane_b32 s10, v200, 8
	v_readlane_b32 s11, v200, 9
	v_readlane_b32 s12, v200, 10
	v_readlane_b32 s13, v200, 11
	v_readlane_b32 s14, v200, 12
	v_readlane_b32 s15, v200, 13
	v_readlane_b32 s16, v200, 14
	v_readlane_b32 s17, v200, 15
	v_readlane_b32 s18, v200, 16
	v_readlane_b32 s19, v200, 17
	v_readlane_b32 s20, v200, 18
	v_readlane_b32 s21, v200, 19
	v_readlane_b32 s22, v200, 20
	v_readlane_b32 s23, v200, 21
	v_readlane_b32 s24, v200, 22
	v_readlane_b32 s25, v200, 23
	v_readlane_b32 s36, v200, 24
	v_readlane_b32 s37, v200, 25
	v_readlane_b32 s38, v200, 26
	v_readlane_b32 s39, v200, 27
	v_readlane_b32 s40, v200, 28
	v_readlane_b32 s41, v200, 29
	v_readlane_b32 s42, v200, 30
	v_readlane_b32 s43, v200, 31
	v_readlane_b32 s44, v200, 32
	v_readlane_b32 s45, v200, 33
	v_readlane_b32 s46, v200, 34
	v_readlane_b32 s47, v200, 35
	v_readlane_b32 s48, v200, 36
	v_readlane_b32 s49, v200, 37
	v_readlane_b32 s50, v200, 38
	v_readlane_b32 s51, v200, 39
	s_nop 1
.Ltc_skip_9:
	v_readlane_b32 s0, v254, 0
	v_readlane_b32 s1, v254, 1
	s_load_dwordx2 s[0:1], s[0:1], 0xd8
	s_waitcnt lgkmcnt(0)
	s_cmp_gt_i32 s1, 23
	s_cselect_b64 s[0:1], -1, 0
	s_and_b64 s[2:3], s[4:5], s[0:1]
	s_andn2_b64 vcc, exec, s[2:3]
	s_cbranch_vccnz .LBB0_2076
	s_waitcnt vmcnt(0)
	s_cmp_gt_u32 s94, 63
	s_barrier
	s_cbranch_scc1 .LBB0_2075
	v_mbcnt_lo_u32_b32 v0, -1, 0
	v_mbcnt_hi_u32_b32 v0, -1, v0
	v_cmp_eq_u32_e32 vcc, 0, v0
	s_and_saveexec_b64 s[2:3], vcc
	s_cbranch_execz .LBB0_2074
	s_add_i32 s4, 0, 0x20020
	v_mov_b32_e32 v0, s4
	s_waitcnt vmcnt(0) expcnt(0) lgkmcnt(0)
	ds_read_b32 v2, v0
	s_add_i32 s4, 0, 0x20024
	v_mov_b32_e32 v0, s4
	ds_read_b32 v0, v0
	s_waitcnt lgkmcnt(1)
	v_cmp_ne_u32_e32 vcc, 0, v2
	s_cbranch_vccnz .LBB0_2038
	v_readlane_b32 s4, v254, 2
	v_readlane_b32 s10, v254, 0
	v_readlane_b32 s5, v254, 3
	v_readlane_b32 s11, v254, 1
	s_load_dwordx2 s[8:9], s[4:5], 0x4
	s_mov_b32 s46, 1
	s_load_dword s10, s[10:11], 0xe8
	s_add_u32 s4, s88, 0x4200
	s_addc_u32 s5, s89, 0
	s_add_u32 s6, s88, 0x4400
	s_addc_u32 s7, s89, 0
	s_waitcnt lgkmcnt(0)
	s_mul_i32 s33, s8, s10
	s_add_u32 s8, s88, 0x4500
	s_mul_i32 s33, s33, s9
	s_addc_u32 s9, s89, 0
	s_add_u32 s10, s88, 0x4600
	s_addc_u32 s11, s89, 0
	s_add_u32 s12, s88, 0x4700
	s_addc_u32 s13, s89, 0
	s_add_u32 s14, s88, 0x4800
	s_addc_u32 s15, s89, 0
	s_add_u32 s16, s88, 0x4900
	s_addc_u32 s17, s89, 0
	s_add_u32 s18, s88, 0x4a00
	s_addc_u32 s19, s89, 0
	s_add_u32 s20, s88, 0x4b00
	s_addc_u32 s21, s89, 0
	s_add_u32 s22, s88, 0x4c00
	s_addc_u32 s23, s89, 0
	s_add_u32 s24, s88, 0x4d00
	s_addc_u32 s25, s89, 0
	s_add_u32 s26, s88, 0x4e00
	s_addc_u32 s27, s89, 0
	s_add_u32 s28, s88, 0x4f00
	s_addc_u32 s29, s89, 0
	s_add_u32 s30, s88, 0x5000
	s_addc_u32 s31, s89, 0
	s_add_u32 s34, s88, 0x5100
	s_addc_u32 s35, s89, 0
	s_add_u32 s36, s88, 0x5200
	s_addc_u32 s37, s89, 0
	s_add_u32 s38, s88, 0x5300
	s_addc_u32 s39, s89, 0
	v_mov_b32_e32 v16, 0
	s_branch .LBB0_2026

.LBB0_2154:
	s_cmp_lt_u32 s96, 32
	s_cbranch_scc1 .Ltc_skip_10
	v_writelane_b32 v200, s0, 0
	s_nop 1
	v_writelane_b32 v200, s1, 1
	s_nop 1
	v_writelane_b32 v200, s2, 2
	s_nop 1
	v_writelane_b32 v200, s3, 3
	s_nop 1
	v_writelane_b32 v200, s4, 4
	s_nop 1
	v_writelane_b32 v200, s5, 5
	s_nop 1
	v_writelane_b32 v200, s6, 6
	s_nop 1
	v_writelane_b32 v200, s7, 7
	s_nop 1
	v_writelane_b32 v200, s10, 8
	s_nop 1
	v_writelane_b32 v200, s11, 9
	s_nop 1
	v_writelane_b32 v200, s12, 10
	s_nop 1
	v_writelane_b32 v200, s13, 11
	s_nop 1
	v_writelane_b32 v200, s14, 12
	s_nop 1
	v_writelane_b32 v200, s15, 13
	s_nop 1
	v_writelane_b32 v200, s16, 14
	s_nop 1
	v_writelane_b32 v200, s17, 15
	s_nop 1
	v_writelane_b32 v200, s18, 16
	s_nop 1
	v_writelane_b32 v200, s19, 17
	s_nop 1
	v_writelane_b32 v200, s20, 18
	s_nop 1
	v_writelane_b32 v200, s21, 19
	s_nop 1
	v_writelane_b32 v200, s22, 20
	s_nop 1
	v_writelane_b32 v200, s23, 21
	s_nop 1
	v_writelane_b32 v200, s24, 22
	s_nop 1
	v_writelane_b32 v200, s25, 23
	s_nop 1
	v_writelane_b32 v200, s36, 24
	s_nop 1
	v_writelane_b32 v200, s37, 25
	s_nop 1
	v_writelane_b32 v200, s38, 26
	s_nop 1
	v_writelane_b32 v200, s39, 27
	s_nop 1
	v_writelane_b32 v200, s40, 28
	s_nop 1
	v_writelane_b32 v200, s41, 29
	s_nop 1
	v_writelane_b32 v200, s42, 30
	s_nop 1
	v_writelane_b32 v200, s43, 31
	s_nop 1
	v_writelane_b32 v200, s44, 32
	s_nop 1
	v_writelane_b32 v200, s45, 33
	s_nop 1
	v_writelane_b32 v200, s46, 34
	s_nop 1
	v_writelane_b32 v200, s47, 35
	s_nop 1
	v_writelane_b32 v200, s48, 36
	s_nop 1
	v_writelane_b32 v200, s49, 37
	s_nop 1
	v_writelane_b32 v200, s50, 38
	s_nop 1
	v_writelane_b32 v200, s51, 39
	s_nop 1
	s_mov_b32 s99, 10
	s_mov_b32 s98, 2
	s_mov_b32 s101, 224
	s_add_i32 s100, s96, 3264
	s_branch .Ltc_s2_back
